# speedup vs baseline: 1.0000x; 1.0000x over previous
.LBB1_61:
	s_or_b64 exec, exec, s[2:3]
	s_nop 8
	v_add_u32_e32 v6, v207, v238
	s_waitcnt lgkmcnt(0)
	s_barrier
	ds_read_b128 v[2:5], v6
	ds_read_b128 v[62:65], v6 offset:32
	ds_read_b128 v[68:71], v6 offset:64
	ds_read_b128 v[72:75], v6 offset:96
	ds_read_b128 v[6:9], v241
	ds_read_b128 v[76:79], v241 offset:32
	ds_read_b128 v[80:83], v241 offset:64
	ds_read_b128 v[84:87], v241 offset:96
	ds_read_b128 v[18:21], v242
	ds_read_b128 v[88:91], v242 offset:32
	ds_read_b128 v[92:95], v242 offset:64
	ds_read_b128 v[96:99], v242 offset:96
	s_waitcnt vmcnt(3) lgkmcnt(11)
	v_mfma_f32_32x32x16_f16 v[34:49], v[2:5], v[100:103], 0
	s_waitcnt lgkmcnt(7)
	v_mfma_f32_32x32x16_f16 v[2:17], v[6:9], v[100:103], 0
	s_waitcnt lgkmcnt(3)
	v_mfma_f32_32x32x16_f16 v[18:33], v[18:21], v[100:103], 0
	s_waitcnt vmcnt(2)
	v_mfma_f32_32x32x16_f16 v[34:49], v[62:65], v[58:61], v[34:49]
	v_mfma_f32_32x32x16_f16 v[2:17], v[76:79], v[58:61], v[2:17]
	s_waitcnt lgkmcnt(2)
	v_mfma_f32_32x32x16_f16 v[18:33], v[88:91], v[58:61], v[18:33]
	s_waitcnt vmcnt(1)
	v_mfma_f32_32x32x16_f16 v[34:49], v[68:71], v[54:57], v[34:49]
	v_mfma_f32_32x32x16_f16 v[2:17], v[80:83], v[54:57], v[2:17]
	s_waitcnt lgkmcnt(1)
	v_mfma_f32_32x32x16_f16 v[18:33], v[92:95], v[54:57], v[18:33]
	s_waitcnt vmcnt(0)
	v_mfma_f32_32x32x16_f16 v[34:49], v[72:75], v[50:53], v[34:49]
	v_mfma_f32_32x32x16_f16 v[2:17], v[84:87], v[50:53], v[2:17]
	s_waitcnt lgkmcnt(0)
	v_mfma_f32_32x32x16_f16 v[18:33], v[96:99], v[50:53], v[18:33]
	v_and_b32_e32 v81, 63, v0
	v_lshl_add_u32 v81, v81, 2, v221
	s_and_saveexec_b64 s[2:3], s[6:7]
	s_xor_b64 s[2:3], exec, s[2:3]
	s_cbranch_execz .LBB1_63
	s_nop 5
	ds_write_b64 v81, v[34:35] offset:0
	ds_write_b64 v81, v[36:37] offset:512
	ds_write_b64 v81, v[38:39] offset:1024
	ds_write_b64 v81, v[40:41] offset:1536
	ds_write_b64 v81, v[42:43] offset:2048
	ds_write_b64 v81, v[44:45] offset:2560
	ds_write_b64 v81, v[46:47] offset:3072
	ds_write_b64 v81, v[48:49] offset:3584
	ds_write_b64 v81, v[2:3] offset:4096
	ds_write_b64 v81, v[4:5] offset:4608
	ds_write_b64 v81, v[6:7] offset:5120
	ds_write_b64 v81, v[8:9] offset:5632
.LBB1_63:
	s_andn2_saveexec_b64 s[2:3], s[2:3]
	s_cbranch_execz .LBB1_65
	s_nop 4
	ds_write_b64 v81, v[10:11] offset:6144
	ds_write_b64 v81, v[12:13] offset:6656
	ds_write_b64 v81, v[14:15] offset:7168
	ds_write_b64 v81, v[16:17] offset:7680
	ds_write_b64 v81, v[18:19] offset:8192
	ds_write_b64 v81, v[20:21] offset:8704
	ds_write_b64 v81, v[22:23] offset:9216
	ds_write_b64 v81, v[24:25] offset:9728
	ds_write_b64 v81, v[26:27] offset:10240
	ds_write_b64 v81, v[28:29] offset:10752

.Lep1_prej:
	s_waitcnt lgkmcnt(7)
	s_barrier
	s_cmp_eq_u64 s[6:7], 0
	s_cbranch_scc0 .Lep1_k1
	s_mul_i32 s43, s36, 0x5000
	s_add_i32 s43, s43, s86
	s_add_u32 s40, s18, s43
	s_addc_u32 s41, s19, 0
	ds_read_b64 v[50:51], v81 offset:0
	ds_read_b64 v[52:53], v81 offset:512
	ds_read_b64 v[54:55], v81 offset:1024
	ds_read_b64 v[56:57], v81 offset:1536
	ds_read_b64 v[58:59], v81 offset:2048
	ds_read_b64 v[60:61], v81 offset:2560
	s_waitcnt lgkmcnt(12)
	v_fma_f32 v78, -v76, v77, 0
	s_waitcnt lgkmcnt(4)
	v_pk_add_f32 v[34:35], v[34:35], v[50:51]
	v_pk_add_f32 v[36:37], v[36:37], v[52:53]
	v_pk_add_f32 v[34:35], v[34:35], v[78:79] op_sel_hi:[1,0]
	v_pk_add_f32 v[36:37], v[36:37], v[78:79] op_sel_hi:[1,0]
	v_pk_fma_f32 v[34:35], v[62:63], v[76:77], v[34:35] op_sel:[0,1,0] op_sel_hi:[1,1,1]
	v_pk_fma_f32 v[36:37], v[64:65], v[76:77], v[36:37] op_sel:[0,1,0] op_sel_hi:[1,1,1]
	v_pk_mul_f32 v[20:21], v[34:35], v[34:35]
	v_pk_add_f32 v[18:19], v[34:35], v[36:37]
	v_pk_fma_f32 v[20:21], v[36:37], v[36:37], v[20:21]
	s_waitcnt lgkmcnt(2)
	v_pk_add_f32 v[38:39], v[38:39], v[54:55]
	v_pk_add_f32 v[40:41], v[40:41], v[56:57]
	v_pk_add_f32 v[38:39], v[38:39], v[78:79] op_sel_hi:[1,0]
	v_pk_add_f32 v[40:41], v[40:41], v[78:79] op_sel_hi:[1,0]
	v_pk_fma_f32 v[38:39], v[68:69], v[76:77], v[38:39] op_sel:[0,1,0] op_sel_hi:[1,1,1]
	v_pk_fma_f32 v[40:41], v[70:71], v[76:77], v[40:41] op_sel:[0,1,0] op_sel_hi:[1,1,1]
	v_pk_add_f32 v[18:19], v[18:19], v[38:39]
	v_pk_fma_f32 v[20:21], v[38:39], v[38:39], v[20:21]
	v_pk_add_f32 v[18:19], v[18:19], v[40:41]
	v_pk_fma_f32 v[20:21], v[40:41], v[40:41], v[20:21]
	s_waitcnt lgkmcnt(0)
	v_pk_add_f32 v[42:43], v[42:43], v[58:59]
	v_pk_add_f32 v[44:45], v[44:45], v[60:61]
	v_pk_add_f32 v[42:43], v[42:43], v[78:79] op_sel_hi:[1,0]
	v_pk_add_f32 v[44:45], v[44:45], v[78:79] op_sel_hi:[1,0]
	v_pk_fma_f32 v[42:43], v[72:73], v[76:77], v[42:43] op_sel:[0,1,0] op_sel_hi:[1,1,1]
	v_pk_fma_f32 v[44:45], v[74:75], v[76:77], v[44:45] op_sel:[0,1,0] op_sel_hi:[1,1,1]
	v_pk_add_f32 v[18:19], v[18:19], v[42:43]
	v_pk_fma_f32 v[20:21], v[42:43], v[42:43], v[20:21]
	v_pk_add_f32 v[18:19], v[18:19], v[44:45]
	v_pk_fma_f32 v[20:21], v[44:45], v[44:45], v[20:21]
	ds_read_b64 v[50:51], v81 offset:3072
	ds_read_b64 v[52:53], v81 offset:3584
	ds_read_b64 v[54:55], v81 offset:4096
	ds_read_b64 v[56:57], v81 offset:4608
	ds_read_b64 v[58:59], v81 offset:5120
	ds_read_b64 v[60:61], v81 offset:5632
	ds_read2st64_b32 v[62:63], v67 offset0:48 offset1:50
	ds_read2st64_b32 v[64:65], v67 offset0:52 offset1:54
	ds_read2st64_b32 v[68:69], v67 offset0:64 offset1:66
	ds_read2st64_b32 v[70:71], v67 offset0:68 offset1:70
	ds_read2st64_b32 v[72:73], v67 offset0:80 offset1:82
	ds_read2st64_b32 v[74:75], v67 offset0:84 offset1:86
	s_barrier
	ds_read_b32 v80, v236
	s_waitcnt lgkmcnt(5)
	v_pk_add_f32 v[46:47], v[46:47], v[50:51]
	v_pk_add_f32 v[48:49], v[48:49], v[52:53]
	v_pk_add_f32 v[46:47], v[46:47], v[78:79] op_sel_hi:[1,0]
	v_pk_add_f32 v[48:49], v[48:49], v[78:79] op_sel_hi:[1,0]
	v_pk_fma_f32 v[46:47], v[62:63], v[76:77], v[46:47] op_sel:[0,1,0] op_sel_hi:[1,1,1]
	v_pk_fma_f32 v[48:49], v[64:65], v[76:77], v[48:49] op_sel:[0,1,0] op_sel_hi:[1,1,1]
	v_pk_add_f32 v[18:19], v[18:19], v[46:47]
	v_pk_fma_f32 v[20:21], v[46:47], v[46:47], v[20:21]
	v_pk_add_f32 v[18:19], v[18:19], v[48:49]
	v_pk_fma_f32 v[20:21], v[48:49], v[48:49], v[20:21]
	s_waitcnt lgkmcnt(3)
	v_pk_add_f32 v[2:3], v[2:3], v[54:55]
	v_pk_add_f32 v[4:5], v[4:5], v[56:57]
	v_pk_add_f32 v[2:3], v[2:3], v[78:79] op_sel_hi:[1,0]
	v_pk_add_f32 v[4:5], v[4:5], v[78:79] op_sel_hi:[1,0]
	v_pk_fma_f32 v[2:3], v[68:69], v[76:77], v[2:3] op_sel:[0,1,0] op_sel_hi:[1,1,1]
	v_pk_fma_f32 v[4:5], v[70:71], v[76:77], v[4:5] op_sel:[0,1,0] op_sel_hi:[1,1,1]
	v_pk_add_f32 v[18:19], v[18:19], v[2:3]
	v_pk_fma_f32 v[20:21], v[2:3], v[2:3], v[20:21]
	v_pk_add_f32 v[18:19], v[18:19], v[4:5]
	v_pk_fma_f32 v[20:21], v[4:5], v[4:5], v[20:21]
	s_waitcnt lgkmcnt(1)
	v_pk_add_f32 v[6:7], v[6:7], v[58:59]
	v_pk_add_f32 v[8:9], v[8:9], v[60:61]
	v_pk_add_f32 v[6:7], v[6:7], v[78:79] op_sel_hi:[1,0]
	v_pk_add_f32 v[8:9], v[8:9], v[78:79] op_sel_hi:[1,0]
	v_pk_fma_f32 v[6:7], v[72:73], v[76:77], v[6:7] op_sel:[0,1,0] op_sel_hi:[1,1,1]
	v_pk_fma_f32 v[8:9], v[74:75], v[76:77], v[8:9] op_sel:[0,1,0] op_sel_hi:[1,1,1]
	v_pk_add_f32 v[18:19], v[18:19], v[6:7]
	v_pk_fma_f32 v[20:21], v[6:7], v[6:7], v[20:21]
	v_pk_add_f32 v[18:19], v[18:19], v[8:9]
	v_pk_fma_f32 v[20:21], v[8:9], v[8:9], v[20:21]
	v_add_f32_e32 v18, v18, v19
	v_add_f32_e32 v20, v20, v21
	s_nop 1
	v_permlane32_swap_b32_e32 v18, v20
	v_add_f32_e32 v22, v18, v20
	s_branch .Lep1_wr0
.Lep1_k1:
	s_setprio 2
	ds_read_b64 v[50:51], v81 offset:6144
	ds_read_b64 v[52:53], v81 offset:6656
	ds_read_b64 v[54:55], v81 offset:7168
	ds_read_b64 v[56:57], v81 offset:7680
	ds_read_b64 v[58:59], v81 offset:8192
	ds_read_b64 v[60:61], v81 offset:8704
	s_waitcnt lgkmcnt(12)
	v_fma_f32 v78, -v76, v77, 0
	s_waitcnt lgkmcnt(4)
	v_pk_add_f32 v[10:11], v[10:11], v[50:51]
	v_pk_add_f32 v[12:13], v[12:13], v[52:53]
	v_pk_add_f32 v[10:11], v[10:11], v[78:79] op_sel_hi:[1,0]
	v_pk_add_f32 v[12:13], v[12:13], v[78:79] op_sel_hi:[1,0]
	v_pk_fma_f32 v[10:11], v[62:63], v[76:77], v[10:11] op_sel:[0,1,0] op_sel_hi:[1,1,1]
	v_pk_fma_f32 v[12:13], v[64:65], v[76:77], v[12:13] op_sel:[0,1,0] op_sel_hi:[1,1,1]
	v_pk_mul_f32 v[36:37], v[10:11], v[10:11]
	v_pk_add_f32 v[34:35], v[10:11], v[12:13]
	v_pk_fma_f32 v[36:37], v[12:13], v[12:13], v[36:37]
	s_waitcnt lgkmcnt(2)
	v_pk_add_f32 v[14:15], v[14:15], v[54:55]
	v_pk_add_f32 v[16:17], v[16:17], v[56:57]
	v_pk_add_f32 v[14:15], v[14:15], v[78:79] op_sel_hi:[1,0]
	v_pk_add_f32 v[16:17], v[16:17], v[78:79] op_sel_hi:[1,0]
	v_pk_fma_f32 v[14:15], v[68:69], v[76:77], v[14:15] op_sel:[0,1,0] op_sel_hi:[1,1,1]
	v_pk_fma_f32 v[16:17], v[70:71], v[76:77], v[16:17] op_sel:[0,1,0] op_sel_hi:[1,1,1]
	v_pk_add_f32 v[34:35], v[34:35], v[14:15]
	v_pk_fma_f32 v[36:37], v[14:15], v[14:15], v[36:37]
	v_pk_add_f32 v[34:35], v[34:35], v[16:17]
	v_pk_fma_f32 v[36:37], v[16:17], v[16:17], v[36:37]
	s_waitcnt lgkmcnt(0)
	v_pk_add_f32 v[18:19], v[18:19], v[58:59]
	v_pk_add_f32 v[20:21], v[20:21], v[60:61]
	v_pk_add_f32 v[18:19], v[18:19], v[78:79] op_sel_hi:[1,0]
	v_pk_add_f32 v[20:21], v[20:21], v[78:79] op_sel_hi:[1,0]
	v_pk_fma_f32 v[18:19], v[72:73], v[76:77], v[18:19] op_sel:[0,1,0] op_sel_hi:[1,1,1]
	v_pk_fma_f32 v[20:21], v[74:75], v[76:77], v[20:21] op_sel:[0,1,0] op_sel_hi:[1,1,1]
	v_pk_add_f32 v[34:35], v[34:35], v[18:19]
	v_pk_fma_f32 v[36:37], v[18:19], v[18:19], v[36:37]
	v_pk_add_f32 v[34:35], v[34:35], v[20:21]
	v_pk_fma_f32 v[36:37], v[20:21], v[20:21], v[36:37]
	ds_read_b64 v[50:51], v81 offset:9216
	ds_read_b64 v[52:53], v81 offset:9728
	ds_read2st64_b32 v[62:63], v67 offset0:144 offset1:146
	ds_read2st64_b32 v[64:65], v67 offset0:148 offset1:150
	s_waitcnt lgkmcnt(0)
	v_pk_add_f32 v[22:23], v[22:23], v[50:51]
	v_pk_add_f32 v[24:25], v[24:25], v[52:53]
	v_pk_add_f32 v[22:23], v[22:23], v[78:79] op_sel_hi:[1,0]
	v_pk_add_f32 v[24:25], v[24:25], v[78:79] op_sel_hi:[1,0]
	v_pk_fma_f32 v[22:23], v[62:63], v[76:77], v[22:23] op_sel:[0,1,0] op_sel_hi:[1,1,1]
	v_pk_fma_f32 v[24:25], v[64:65], v[76:77], v[24:25] op_sel:[0,1,0] op_sel_hi:[1,1,1]
	v_pk_add_f32 v[34:35], v[34:35], v[22:23]
	v_pk_fma_f32 v[36:37], v[22:23], v[22:23], v[36:37]
	v_pk_add_f32 v[34:35], v[34:35], v[24:25]
	v_pk_fma_f32 v[36:37], v[24:25], v[24:25], v[36:37]
	s_mov_b64 s[40:41], exec
	s_and_b64 exec, exec, s[0:1]
	ds_read_b64 v[50:51], v81 offset:10240
	ds_read_b64 v[52:53], v81 offset:10752
	ds_read2st64_b32 v[62:63], v67 offset0:160 offset1:162
	ds_read2st64_b32 v[64:65], v67 offset0:164 offset1:166
	s_waitcnt lgkmcnt(0)
	v_pk_add_f32 v[26:27], v[26:27], v[50:51]
	v_pk_add_f32 v[28:29], v[28:29], v[52:53]
	v_pk_add_f32 v[26:27], v[26:27], v[78:79] op_sel_hi:[1,0]
	v_pk_add_f32 v[28:29], v[28:29], v[78:79] op_sel_hi:[1,0]
	v_pk_fma_f32 v[26:27], v[62:63], v[76:77], v[26:27] op_sel:[0,1,0] op_sel_hi:[1,1,1]
	v_pk_fma_f32 v[28:29], v[64:65], v[76:77], v[28:29] op_sel:[0,1,0] op_sel_hi:[1,1,1]
	v_pk_add_f32 v[34:35], v[34:35], v[26:27]
	v_pk_fma_f32 v[36:37], v[26:27], v[26:27], v[36:37]
	v_pk_add_f32 v[34:35], v[34:35], v[28:29]
	v_pk_fma_f32 v[36:37], v[28:29], v[28:29], v[36:37]
	s_mov_b64 exec, s[40:41]
	v_add_f32_e32 v34, v34, v35
	v_add_f32_e32 v36, v36, v37
	s_nop 1
	v_permlane32_swap_b32_e32 v34, v36
	v_add_f32_e32 v38, v34, v36
	ds_write_b32 v236, v38

.LBB1_142:
	s_or_b64 exec, exec, s[2:3]
	s_nop 8
	v_add_co_u32_e32 v2, vcc, 0x2000, v174
	s_nop 1
	v_addc_co_u32_e32 v3, vcc, 0, v175, vcc
	global_load_dwordx4 v[68:71], v[2:3], off
	global_load_dwordx4 v[72:75], v[2:3], off offset:1024
	global_load_dwordx4 v[84:87], v[2:3], off offset:2048
	global_load_dwordx4 v[88:91], v[2:3], off offset:3072
	v_add_co_u32_e32 v2, vcc, 0x3000, v174
	s_nop 1
	v_addc_co_u32_e32 v3, vcc, 0, v175, vcc
	global_load_dwordx4 v[92:95], v[2:3], off
	global_load_dwordx4 v[96:99], v[2:3], off offset:1024
	global_load_dwordx4 v[100:103], v[2:3], off offset:2048
	global_load_dwordx4 v[104:107], v[2:3], off offset:3072
	s_waitcnt lgkmcnt(0)
	s_barrier
	ds_read_b128 v[2:5], v245 offset:33280
	ds_read_b128 v[108:111], v245 offset:33312
	ds_read_b128 v[18:21], v246
	ds_read_b128 v[112:115], v246 offset:32
	ds_read_b128 v[116:119], v245 offset:32
	ds_read_b128 v[120:123], v245 offset:64
	ds_read_b128 v[6:9], v245
	ds_read_b128 v[124:127], v245 offset:33344
	ds_read_b128 v[128:131], v246 offset:64
	s_waitcnt vmcnt(15) lgkmcnt(2)
	v_mfma_f32_32x32x16_f16 v[34:49], v[6:9], v[136:139], 0
	v_mfma_f32_32x32x16_f16 v[2:17], v[2:5], v[136:139], 0
	v_mfma_f32_32x32x16_f16 v[18:33], v[18:21], v[136:139], 0
	ds_read_b128 v[136:139], v245 offset:96
	ds_read_b128 v[140:143], v245 offset:33376
	ds_read_b128 v[144:147], v246 offset:96
	s_waitcnt vmcnt(14)
	v_mfma_f32_32x32x16_f16 v[34:49], v[116:119], v[132:135], v[34:49]
	v_mfma_f32_32x32x16_f16 v[2:17], v[108:111], v[132:135], v[2:17]
	v_mfma_f32_32x32x16_f16 v[18:33], v[112:115], v[132:135], v[18:33]
	ds_read_b128 v[108:111], v245 offset:128
	ds_read_b128 v[112:115], v245 offset:33408
	ds_read_b128 v[116:119], v246 offset:128
	s_waitcnt vmcnt(13)
	v_mfma_f32_32x32x16_f16 v[34:49], v[120:123], v[80:83], v[34:49]
	s_waitcnt lgkmcnt(7)
	v_mfma_f32_32x32x16_f16 v[2:17], v[124:127], v[80:83], v[2:17]
	s_waitcnt lgkmcnt(6)
	v_mfma_f32_32x32x16_f16 v[18:33], v[128:131], v[80:83], v[18:33]
	ds_read_b128 v[80:83], v245 offset:160
	ds_read_b128 v[120:123], v245 offset:33440
	ds_read_b128 v[124:127], v246 offset:160
	s_waitcnt vmcnt(12) lgkmcnt(8)
	v_mfma_f32_32x32x16_f16 v[34:49], v[136:139], v[76:79], v[34:49]
	s_waitcnt lgkmcnt(7)
	v_mfma_f32_32x32x16_f16 v[2:17], v[140:143], v[76:79], v[2:17]
	s_waitcnt lgkmcnt(6)
	v_mfma_f32_32x32x16_f16 v[18:33], v[144:147], v[76:79], v[18:33]
	ds_read_b128 v[76:79], v245 offset:192
	ds_read_b128 v[128:131], v245 offset:33472
	ds_read_b128 v[132:135], v246 offset:192
	s_waitcnt vmcnt(11) lgkmcnt(8)
	v_mfma_f32_32x32x16_f16 v[34:49], v[108:111], v[62:65], v[34:49]
	s_waitcnt lgkmcnt(7)
	v_mfma_f32_32x32x16_f16 v[2:17], v[112:115], v[62:65], v[2:17]
	s_waitcnt lgkmcnt(6)
	v_mfma_f32_32x32x16_f16 v[18:33], v[116:119], v[62:65], v[18:33]
	ds_read_b128 v[62:65], v245 offset:224
	ds_read_b128 v[108:111], v245 offset:33504
	ds_read_b128 v[112:115], v246 offset:224
	s_waitcnt vmcnt(10) lgkmcnt(8)
	v_mfma_f32_32x32x16_f16 v[34:49], v[80:83], v[58:61], v[34:49]
	s_waitcnt lgkmcnt(7)
	v_mfma_f32_32x32x16_f16 v[2:17], v[120:123], v[58:61], v[2:17]
	s_waitcnt lgkmcnt(6)
	v_mfma_f32_32x32x16_f16 v[18:33], v[124:127], v[58:61], v[18:33]
	ds_read_b128 v[58:61], v245 offset:256
	ds_read_b128 v[80:83], v245 offset:33536
	ds_read_b128 v[116:119], v246 offset:256
	s_waitcnt vmcnt(9) lgkmcnt(8)
	v_mfma_f32_32x32x16_f16 v[34:49], v[76:79], v[54:57], v[34:49]
	s_waitcnt lgkmcnt(7)
	v_mfma_f32_32x32x16_f16 v[2:17], v[128:131], v[54:57], v[2:17]
	s_waitcnt lgkmcnt(6)
	v_mfma_f32_32x32x16_f16 v[18:33], v[132:135], v[54:57], v[18:33]
	ds_read_b128 v[54:57], v245 offset:288
	ds_read_b128 v[76:79], v245 offset:33568
	ds_read_b128 v[120:123], v246 offset:288
	s_waitcnt vmcnt(8) lgkmcnt(8)
	v_mfma_f32_32x32x16_f16 v[34:49], v[62:65], v[50:53], v[34:49]
	s_waitcnt lgkmcnt(7)
	v_mfma_f32_32x32x16_f16 v[2:17], v[108:111], v[50:53], v[2:17]
	s_waitcnt lgkmcnt(6)
	v_mfma_f32_32x32x16_f16 v[18:33], v[112:115], v[50:53], v[18:33]
	ds_read_b128 v[50:53], v245 offset:320
	ds_read_b128 v[62:65], v245 offset:33600
	ds_read_b128 v[108:111], v246 offset:320
	s_waitcnt vmcnt(7) lgkmcnt(8)
	v_mfma_f32_32x32x16_f16 v[34:49], v[58:61], v[68:71], v[34:49]
	s_waitcnt lgkmcnt(7)
	v_mfma_f32_32x32x16_f16 v[2:17], v[80:83], v[68:71], v[2:17]
	s_waitcnt lgkmcnt(6)
	v_mfma_f32_32x32x16_f16 v[18:33], v[116:119], v[68:71], v[18:33]
	ds_read_b128 v[58:61], v245 offset:352
	ds_read_b128 v[68:71], v245 offset:33632
	ds_read_b128 v[80:83], v246 offset:352
	s_waitcnt vmcnt(6) lgkmcnt(8)
	v_mfma_f32_32x32x16_f16 v[34:49], v[54:57], v[72:75], v[34:49]
	s_waitcnt lgkmcnt(7)
	v_mfma_f32_32x32x16_f16 v[2:17], v[76:79], v[72:75], v[2:17]
	s_waitcnt lgkmcnt(6)
	v_mfma_f32_32x32x16_f16 v[18:33], v[120:123], v[72:75], v[18:33]
	ds_read_b128 v[54:57], v245 offset:384
	ds_read_b128 v[72:75], v245 offset:33664
	ds_read_b128 v[76:79], v246 offset:384
	s_waitcnt vmcnt(5) lgkmcnt(8)
	v_mfma_f32_32x32x16_f16 v[34:49], v[50:53], v[84:87], v[34:49]
	s_waitcnt lgkmcnt(7)
	v_mfma_f32_32x32x16_f16 v[2:17], v[62:65], v[84:87], v[2:17]
	s_waitcnt lgkmcnt(6)
	v_mfma_f32_32x32x16_f16 v[18:33], v[108:111], v[84:87], v[18:33]
	ds_read_b128 v[50:53], v245 offset:416
	ds_read_b128 v[62:65], v245 offset:33696
	ds_read_b128 v[84:87], v246 offset:416
	s_waitcnt vmcnt(4) lgkmcnt(8)
	v_mfma_f32_32x32x16_f16 v[34:49], v[58:61], v[88:91], v[34:49]
	s_waitcnt lgkmcnt(7)
	v_mfma_f32_32x32x16_f16 v[2:17], v[68:71], v[88:91], v[2:17]
	s_waitcnt lgkmcnt(6)
	v_mfma_f32_32x32x16_f16 v[18:33], v[80:83], v[88:91], v[18:33]
	ds_read_b128 v[58:61], v245 offset:448
	ds_read_b128 v[68:71], v245 offset:33728
	ds_read_b128 v[80:83], v246 offset:448
	s_waitcnt vmcnt(3) lgkmcnt(8)
	v_mfma_f32_32x32x16_f16 v[34:49], v[54:57], v[92:95], v[34:49]
	s_waitcnt lgkmcnt(7)
	v_mfma_f32_32x32x16_f16 v[2:17], v[72:75], v[92:95], v[2:17]
	s_waitcnt lgkmcnt(6)
	v_mfma_f32_32x32x16_f16 v[18:33], v[76:79], v[92:95], v[18:33]
	ds_read_b128 v[54:57], v245 offset:480
	ds_read_b128 v[72:75], v245 offset:33760
	ds_read_b128 v[76:79], v246 offset:480
	s_waitcnt vmcnt(2) lgkmcnt(8)
	v_mfma_f32_32x32x16_f16 v[34:49], v[50:53], v[96:99], v[34:49]
	s_waitcnt lgkmcnt(7)
	v_mfma_f32_32x32x16_f16 v[2:17], v[62:65], v[96:99], v[2:17]
	s_waitcnt lgkmcnt(6)
	v_mfma_f32_32x32x16_f16 v[18:33], v[84:87], v[96:99], v[18:33]
	s_waitcnt vmcnt(1) lgkmcnt(5)
	v_mfma_f32_32x32x16_f16 v[34:49], v[58:61], v[100:103], v[34:49]
	s_waitcnt lgkmcnt(4)
	v_mfma_f32_32x32x16_f16 v[2:17], v[68:71], v[100:103], v[2:17]
	s_waitcnt lgkmcnt(3)
	v_mfma_f32_32x32x16_f16 v[18:33], v[80:83], v[100:103], v[18:33]
	s_waitcnt vmcnt(0) lgkmcnt(2)
	v_mfma_f32_32x32x16_f16 v[34:49], v[54:57], v[104:107], v[34:49]
	s_waitcnt lgkmcnt(1)
	v_mfma_f32_32x32x16_f16 v[2:17], v[72:75], v[104:107], v[2:17]
	s_waitcnt lgkmcnt(0)
	v_mfma_f32_32x32x16_f16 v[18:33], v[76:79], v[104:107], v[18:33]
	s_barrier
	v_and_b32_e32 v81, 63, v0
	v_lshl_add_u32 v81, v81, 2, v221
	s_and_saveexec_b64 s[2:3], s[6:7]
	s_xor_b64 s[2:3], exec, s[2:3]
	s_cbranch_execz .LBB1_144
	s_nop 3
	ds_write_b64 v81, v[34:35] offset:0
	ds_write_b64 v81, v[36:37] offset:512
	ds_write_b64 v81, v[38:39] offset:1024
	ds_write_b64 v81, v[40:41] offset:1536
	ds_write_b64 v81, v[42:43] offset:2048
	ds_write_b64 v81, v[44:45] offset:2560
	ds_write_b64 v81, v[46:47] offset:3072
	ds_write_b64 v81, v[48:49] offset:3584
	ds_write_b64 v81, v[2:3] offset:4096
	ds_write_b64 v81, v[4:5] offset:4608
	ds_write_b64 v81, v[6:7] offset:5120
	ds_write_b64 v81, v[8:9] offset:5632
.LBB1_144:
	s_andn2_saveexec_b64 s[2:3], s[2:3]
	s_cbranch_execz .LBB1_146
	s_nop 3
	ds_write_b64 v81, v[10:11] offset:6144
	ds_write_b64 v81, v[12:13] offset:6656
	ds_write_b64 v81, v[14:15] offset:7168
	ds_write_b64 v81, v[16:17] offset:7680
	ds_write_b64 v81, v[18:19] offset:8192
	ds_write_b64 v81, v[20:21] offset:8704
	ds_write_b64 v81, v[22:23] offset:9216
	ds_write_b64 v81, v[24:25] offset:9728
	ds_write_b64 v81, v[26:27] offset:10240
	ds_write_b64 v81, v[28:29] offset:10752

.Lep2_prej:
	s_waitcnt lgkmcnt(7)
	s_barrier
	s_cmp_eq_u64 s[6:7], 0
	s_cbranch_scc0 .Lep2_k1
	s_mul_i32 s43, s36, 0x5000
	s_addk_i32 s43, 0x2800
	s_add_i32 s43, s43, s86
	s_add_u32 s40, s18, s43
	s_addc_u32 s41, s19, 0
	ds_read_b64 v[50:51], v81 offset:0
	ds_read_b64 v[52:53], v81 offset:512
	ds_read_b64 v[54:55], v81 offset:1024
	ds_read_b64 v[56:57], v81 offset:1536
	ds_read_b64 v[58:59], v81 offset:2048
	ds_read_b64 v[60:61], v81 offset:2560
	s_waitcnt lgkmcnt(12)
	v_fma_f32 v78, -v76, v77, v173
	s_waitcnt lgkmcnt(4)
	v_pk_add_f32 v[34:35], v[34:35], v[50:51]
	v_pk_add_f32 v[36:37], v[36:37], v[52:53]
	v_pk_add_f32 v[34:35], v[34:35], v[78:79] op_sel_hi:[1,0]
	v_pk_add_f32 v[36:37], v[36:37], v[78:79] op_sel_hi:[1,0]
	v_pk_fma_f32 v[34:35], v[62:63], v[76:77], v[34:35] op_sel:[0,1,0] op_sel_hi:[1,1,1]
	v_pk_fma_f32 v[36:37], v[64:65], v[76:77], v[36:37] op_sel:[0,1,0] op_sel_hi:[1,1,1]
	v_pk_mul_f32 v[20:21], v[34:35], v[34:35]
	v_pk_add_f32 v[18:19], v[34:35], v[36:37]
	v_pk_fma_f32 v[20:21], v[36:37], v[36:37], v[20:21]
	s_waitcnt lgkmcnt(2)
	v_pk_add_f32 v[38:39], v[38:39], v[54:55]
	v_pk_add_f32 v[40:41], v[40:41], v[56:57]
	v_pk_add_f32 v[38:39], v[38:39], v[78:79] op_sel_hi:[1,0]
	v_pk_add_f32 v[40:41], v[40:41], v[78:79] op_sel_hi:[1,0]
	v_pk_fma_f32 v[38:39], v[68:69], v[76:77], v[38:39] op_sel:[0,1,0] op_sel_hi:[1,1,1]
	v_pk_fma_f32 v[40:41], v[70:71], v[76:77], v[40:41] op_sel:[0,1,0] op_sel_hi:[1,1,1]
	v_pk_add_f32 v[18:19], v[18:19], v[38:39]
	v_pk_fma_f32 v[20:21], v[38:39], v[38:39], v[20:21]
	v_pk_add_f32 v[18:19], v[18:19], v[40:41]
	v_pk_fma_f32 v[20:21], v[40:41], v[40:41], v[20:21]
	s_waitcnt lgkmcnt(0)
	v_pk_add_f32 v[42:43], v[42:43], v[58:59]
	v_pk_add_f32 v[44:45], v[44:45], v[60:61]
	v_pk_add_f32 v[42:43], v[42:43], v[78:79] op_sel_hi:[1,0]
	v_pk_add_f32 v[44:45], v[44:45], v[78:79] op_sel_hi:[1,0]
	v_pk_fma_f32 v[42:43], v[72:73], v[76:77], v[42:43] op_sel:[0,1,0] op_sel_hi:[1,1,1]
	v_pk_fma_f32 v[44:45], v[74:75], v[76:77], v[44:45] op_sel:[0,1,0] op_sel_hi:[1,1,1]
	v_pk_add_f32 v[18:19], v[18:19], v[42:43]
	v_pk_fma_f32 v[20:21], v[42:43], v[42:43], v[20:21]
	v_pk_add_f32 v[18:19], v[18:19], v[44:45]
	v_pk_fma_f32 v[20:21], v[44:45], v[44:45], v[20:21]
	ds_read_b64 v[50:51], v81 offset:3072
	ds_read_b64 v[52:53], v81 offset:3584
	ds_read_b64 v[54:55], v81 offset:4096
	ds_read_b64 v[56:57], v81 offset:4608
	ds_read_b64 v[58:59], v81 offset:5120
	ds_read_b64 v[60:61], v81 offset:5632
	ds_read2st64_b32 v[62:63], v67 offset0:48 offset1:50
	ds_read2st64_b32 v[64:65], v67 offset0:52 offset1:54
	ds_read2st64_b32 v[68:69], v67 offset0:64 offset1:66
	ds_read2st64_b32 v[70:71], v67 offset0:68 offset1:70
	ds_read2st64_b32 v[72:73], v67 offset0:80 offset1:82
	ds_read2st64_b32 v[74:75], v67 offset0:84 offset1:86
	s_barrier
	ds_read_b32 v80, v236
	s_waitcnt lgkmcnt(5)
	v_pk_add_f32 v[46:47], v[46:47], v[50:51]
	v_pk_add_f32 v[48:49], v[48:49], v[52:53]
	v_pk_add_f32 v[46:47], v[46:47], v[78:79] op_sel_hi:[1,0]
	v_pk_add_f32 v[48:49], v[48:49], v[78:79] op_sel_hi:[1,0]
	v_pk_fma_f32 v[46:47], v[62:63], v[76:77], v[46:47] op_sel:[0,1,0] op_sel_hi:[1,1,1]
	v_pk_fma_f32 v[48:49], v[64:65], v[76:77], v[48:49] op_sel:[0,1,0] op_sel_hi:[1,1,1]
	v_pk_add_f32 v[18:19], v[18:19], v[46:47]
	v_pk_fma_f32 v[20:21], v[46:47], v[46:47], v[20:21]
	v_pk_add_f32 v[18:19], v[18:19], v[48:49]
	v_pk_fma_f32 v[20:21], v[48:49], v[48:49], v[20:21]
	s_waitcnt lgkmcnt(3)
	v_pk_add_f32 v[2:3], v[2:3], v[54:55]
	v_pk_add_f32 v[4:5], v[4:5], v[56:57]
	v_pk_add_f32 v[2:3], v[2:3], v[78:79] op_sel_hi:[1,0]
	v_pk_add_f32 v[4:5], v[4:5], v[78:79] op_sel_hi:[1,0]
	v_pk_fma_f32 v[2:3], v[68:69], v[76:77], v[2:3] op_sel:[0,1,0] op_sel_hi:[1,1,1]
	v_pk_fma_f32 v[4:5], v[70:71], v[76:77], v[4:5] op_sel:[0,1,0] op_sel_hi:[1,1,1]
	v_pk_add_f32 v[18:19], v[18:19], v[2:3]
	v_pk_fma_f32 v[20:21], v[2:3], v[2:3], v[20:21]
	v_pk_add_f32 v[18:19], v[18:19], v[4:5]
	v_pk_fma_f32 v[20:21], v[4:5], v[4:5], v[20:21]
	s_waitcnt lgkmcnt(1)
	v_pk_add_f32 v[6:7], v[6:7], v[58:59]
	v_pk_add_f32 v[8:9], v[8:9], v[60:61]
	v_pk_add_f32 v[6:7], v[6:7], v[78:79] op_sel_hi:[1,0]
	v_pk_add_f32 v[8:9], v[8:9], v[78:79] op_sel_hi:[1,0]
	v_pk_fma_f32 v[6:7], v[72:73], v[76:77], v[6:7] op_sel:[0,1,0] op_sel_hi:[1,1,1]
	v_pk_fma_f32 v[8:9], v[74:75], v[76:77], v[8:9] op_sel:[0,1,0] op_sel_hi:[1,1,1]
	v_pk_add_f32 v[18:19], v[18:19], v[6:7]
	v_pk_fma_f32 v[20:21], v[6:7], v[6:7], v[20:21]
	v_pk_add_f32 v[18:19], v[18:19], v[8:9]
	v_pk_fma_f32 v[20:21], v[8:9], v[8:9], v[20:21]
	v_add_f32_e32 v18, v18, v19
	v_add_f32_e32 v20, v20, v21
	s_nop 1
	v_permlane32_swap_b32_e32 v18, v20
	v_add_f32_e32 v22, v18, v20
	s_branch .Lep2_wr0
.Lep2_k1:
	s_setprio 2
	ds_read_b64 v[50:51], v81 offset:6144
	ds_read_b64 v[52:53], v81 offset:6656
	ds_read_b64 v[54:55], v81 offset:7168
	ds_read_b64 v[56:57], v81 offset:7680
	ds_read_b64 v[58:59], v81 offset:8192
	ds_read_b64 v[60:61], v81 offset:8704
	s_waitcnt lgkmcnt(12)
	v_fma_f32 v78, -v76, v77, v173
	s_waitcnt lgkmcnt(4)
	v_pk_add_f32 v[10:11], v[10:11], v[50:51]
	v_pk_add_f32 v[12:13], v[12:13], v[52:53]
	v_pk_add_f32 v[10:11], v[10:11], v[78:79] op_sel_hi:[1,0]
	v_pk_add_f32 v[12:13], v[12:13], v[78:79] op_sel_hi:[1,0]
	v_pk_fma_f32 v[10:11], v[62:63], v[76:77], v[10:11] op_sel:[0,1,0] op_sel_hi:[1,1,1]
	v_pk_fma_f32 v[12:13], v[64:65], v[76:77], v[12:13] op_sel:[0,1,0] op_sel_hi:[1,1,1]
	v_pk_mul_f32 v[36:37], v[10:11], v[10:11]
	v_pk_add_f32 v[34:35], v[10:11], v[12:13]
	v_pk_fma_f32 v[36:37], v[12:13], v[12:13], v[36:37]
	s_waitcnt lgkmcnt(2)
	v_pk_add_f32 v[14:15], v[14:15], v[54:55]
	v_pk_add_f32 v[16:17], v[16:17], v[56:57]
	v_pk_add_f32 v[14:15], v[14:15], v[78:79] op_sel_hi:[1,0]
	v_pk_add_f32 v[16:17], v[16:17], v[78:79] op_sel_hi:[1,0]
	v_pk_fma_f32 v[14:15], v[68:69], v[76:77], v[14:15] op_sel:[0,1,0] op_sel_hi:[1,1,1]
	v_pk_fma_f32 v[16:17], v[70:71], v[76:77], v[16:17] op_sel:[0,1,0] op_sel_hi:[1,1,1]
	v_pk_add_f32 v[34:35], v[34:35], v[14:15]
	v_pk_fma_f32 v[36:37], v[14:15], v[14:15], v[36:37]
	v_pk_add_f32 v[34:35], v[34:35], v[16:17]
	v_pk_fma_f32 v[36:37], v[16:17], v[16:17], v[36:37]
	s_waitcnt lgkmcnt(0)
	v_pk_add_f32 v[18:19], v[18:19], v[58:59]
	v_pk_add_f32 v[20:21], v[20:21], v[60:61]
	v_pk_add_f32 v[18:19], v[18:19], v[78:79] op_sel_hi:[1,0]
	v_pk_add_f32 v[20:21], v[20:21], v[78:79] op_sel_hi:[1,0]
	v_pk_fma_f32 v[18:19], v[72:73], v[76:77], v[18:19] op_sel:[0,1,0] op_sel_hi:[1,1,1]
	v_pk_fma_f32 v[20:21], v[74:75], v[76:77], v[20:21] op_sel:[0,1,0] op_sel_hi:[1,1,1]
	v_pk_add_f32 v[34:35], v[34:35], v[18:19]
	v_pk_fma_f32 v[36:37], v[18:19], v[18:19], v[36:37]
	v_pk_add_f32 v[34:35], v[34:35], v[20:21]
	v_pk_fma_f32 v[36:37], v[20:21], v[20:21], v[36:37]
	ds_read_b64 v[50:51], v81 offset:9216
	ds_read_b64 v[52:53], v81 offset:9728
	ds_read2st64_b32 v[62:63], v67 offset0:144 offset1:146
	ds_read2st64_b32 v[64:65], v67 offset0:148 offset1:150
	s_waitcnt lgkmcnt(0)
	v_pk_add_f32 v[22:23], v[22:23], v[50:51]
	v_pk_add_f32 v[24:25], v[24:25], v[52:53]
	v_pk_add_f32 v[22:23], v[22:23], v[78:79] op_sel_hi:[1,0]
	v_pk_add_f32 v[24:25], v[24:25], v[78:79] op_sel_hi:[1,0]
	v_pk_fma_f32 v[22:23], v[62:63], v[76:77], v[22:23] op_sel:[0,1,0] op_sel_hi:[1,1,1]
	v_pk_fma_f32 v[24:25], v[64:65], v[76:77], v[24:25] op_sel:[0,1,0] op_sel_hi:[1,1,1]
	v_pk_add_f32 v[34:35], v[34:35], v[22:23]
	v_pk_fma_f32 v[36:37], v[22:23], v[22:23], v[36:37]
	v_pk_add_f32 v[34:35], v[34:35], v[24:25]
	v_pk_fma_f32 v[36:37], v[24:25], v[24:25], v[36:37]
	s_mov_b64 s[40:41], exec
	s_and_b64 exec, exec, s[0:1]
	ds_read_b64 v[50:51], v81 offset:10240
	ds_read_b64 v[52:53], v81 offset:10752
	ds_read2st64_b32 v[62:63], v67 offset0:160 offset1:162
	ds_read2st64_b32 v[64:65], v67 offset0:164 offset1:166
	s_waitcnt lgkmcnt(0)
	v_pk_add_f32 v[26:27], v[26:27], v[50:51]
	v_pk_add_f32 v[28:29], v[28:29], v[52:53]
	v_pk_add_f32 v[26:27], v[26:27], v[78:79] op_sel_hi:[1,0]
	v_pk_add_f32 v[28:29], v[28:29], v[78:79] op_sel_hi:[1,0]
	v_pk_fma_f32 v[26:27], v[62:63], v[76:77], v[26:27] op_sel:[0,1,0] op_sel_hi:[1,1,1]
	v_pk_fma_f32 v[28:29], v[64:65], v[76:77], v[28:29] op_sel:[0,1,0] op_sel_hi:[1,1,1]
	v_pk_add_f32 v[34:35], v[34:35], v[26:27]
	v_pk_fma_f32 v[36:37], v[26:27], v[26:27], v[36:37]
	v_pk_add_f32 v[34:35], v[34:35], v[28:29]
	v_pk_fma_f32 v[36:37], v[28:29], v[28:29], v[36:37]
	s_mov_b64 exec, s[40:41]
	v_add_f32_e32 v34, v34, v35
	v_add_f32_e32 v36, v36, v37
	s_nop 1
	v_permlane32_swap_b32_e32 v34, v36
	v_add_f32_e32 v38, v34, v36
	ds_write_b32 v236, v38
